# grid barrier: acquiring L1 invalidate issued before the spin (completes under the wait) instead of after the release is seen
# speedup vs baseline: 1.0199x; 1.0069x over previous
; __device__ __forceinline__ unsigned xb_ld(unsigned* p)              { return __hip_atomic_load(p, __ATOMIC_RELAXED, __HIP_MEMORY_SCOPE_AGENT); }
; __device__ __forceinline__ unsigned xb_add(unsigned* p, unsigned v) { return __hip_atomic_fetch_add(p, v, __ATOMIC_RELAXED, __HIP_MEMORY_SCOPE_AGENT); }
; #define XB_SPIN(cond, bar) do { unsigned _sp = 0; while (cond) { __builtin_amdgcn_s_sleep(1); \
;     if ((++_sp & 255u) == 0u) { if (xb_ld(&(bar)[XB_TMO])) break; if (_sp > XB_SPIN_CAP) { atomicAdd(&(bar)[XB_TMO], 1u); break; } } } } while (0)
; __device__ __forceinline__ void xcd_barrier(const XcdBarrier& b) {
;     ...
;     if (threadIdx.x == 0) {
;         unsigned* bar = b.bar;
;         __builtin_amdgcn_s_waitcnt(0);
;         unsigned nloc = b.st[0], nx = b.st[1];
;         if (nloc == 0u) { xcd_barrier_complete(bar, b.x, nloc, nx); b.st[0] = nloc; b.st[1] = nx; }
;         const unsigned old = xb_add(&bar[XB_XSUB(b.x)], 1u);
;         const unsigned gen = old / nloc;
;         if (old + 1u == (gen + 1u) * nloc) {
;             __builtin_amdgcn_fence(__ATOMIC_RELEASE, "agent");
;             asm volatile("s_waitcnt vmcnt(0)" ::: "memory");
;             const unsigned og = xb_add(&bar[XB_TOP], 1u);
;             const unsigned tg = og / nx;
;             if (og + 1u == (tg + 1u) * nx) xb_add(&bar[XB_TOPGEN], 1u);
;             else XB_SPIN(xb_ld(&bar[XB_TOPGEN]) == tg, bar);
;             __builtin_amdgcn_fence(__ATOMIC_ACQUIRE, "agent");
;             xb_add(&bar[XB_XGEN(b.x)], 1u);
;             asm volatile("s_waitcnt vmcnt(0)" ::: "memory");
;         } else {
;             XB_SPIN(xb_ld(&bar[XB_XGEN(b.x)]) == gen, bar);
.LBB0_68:
	s_lshl_b32 s3, s86, 8
	s_add_u32 s4, s72, s3
	s_addc_u32 s5, s73, 0
	v_mov_b32_e32 v2, 0x1000
	v_mov_b32_e32 v4, 1
	global_atomic_add v4, v2, v4, s[4:5] offset:1024 sc0
	v_cvt_f32_u32_e32 v2, v3
	v_sub_u32_e32 v5, 0, v3
	v_rcp_iflag_f32_e32 v2, v2
	s_nop 0
	v_mul_f32_e32 v2, 0x4f7ffffe, v2
	v_cvt_u32_f32_e32 v2, v2
	v_mul_lo_u32 v5, v5, v2
	v_mul_hi_u32 v5, v2, v5
	v_add_u32_e32 v2, v2, v5
	s_waitcnt vmcnt(0)
	v_mul_hi_u32 v2, v4, v2
	v_mul_lo_u32 v5, v2, v3
	v_sub_u32_e32 v5, v4, v5
	v_add_u32_e32 v6, 1, v2
	v_cmp_ge_u32_e32 vcc, v5, v3
	v_add_u32_e32 v4, 1, v4
	s_nop 0
	v_cndmask_b32_e32 v2, v2, v6, vcc
	v_sub_u32_e32 v6, v5, v3
	v_cndmask_b32_e32 v5, v5, v6, vcc
	v_add_u32_e32 v6, 1, v2
	v_cmp_ge_u32_e32 vcc, v5, v3
	s_nop 1
	v_cndmask_b32_e32 v2, v2, v6, vcc
	v_mul_lo_u32 v5, v3, v2
	v_add_u32_e32 v3, v5, v3
	v_cmp_ne_u32_e32 vcc, v4, v3
	s_and_saveexec_b64 s[6:7], vcc
	s_xor_b64 s[6:7], exec, s[6:7]
	s_cbranch_execz .LBB0_82
	s_waitcnt lgkmcnt(0)
	buffer_inv sc1
	v_mov_b32_e32 v1, 0x2000
	global_load_dword v1, v1, s[4:5] offset:1024 sc1
	s_add_u32 s10, s4, 0x2400
	s_addc_u32 s11, s5, 0
	s_waitcnt vmcnt(0)
	v_cmp_eq_u32_e32 vcc, v1, v2
	s_and_saveexec_b64 s[8:9], vcc
	s_cbranch_execz .LBB0_81
	s_mov_b32 s3, 1
	s_mov_b64 s[28:29], 0
	v_mov_b32_e32 v1, 0
	s_branch .LBB0_72

; __device__ __forceinline__ unsigned xb_add(unsigned* p, unsigned v) { return __hip_atomic_fetch_add(p, v, __ATOMIC_RELAXED, __HIP_MEMORY_SCOPE_AGENT); }
; __device__ __forceinline__ void xcd_barrier(const XcdBarrier& b) {
;     ...
;         const unsigned gen = old / nloc;
;         if (old + 1u == (gen + 1u) * nloc) {
;             __builtin_amdgcn_fence(__ATOMIC_RELEASE, "agent");
;             asm volatile("s_waitcnt vmcnt(0)" ::: "memory");
;             const unsigned og = xb_add(&bar[XB_TOP], 1u);
.LBB0_81:
	s_or_b64 exec, exec, s[8:9]
	s_waitcnt vmcnt(0)
	s_waitcnt vmcnt(0)
.LBB0_82:
	s_andn2_saveexec_b64 s[6:7], s[6:7]
	s_cbranch_execz .LBB0_100
	s_mov_b64 s[6:7], exec
	buffer_wbl2 sc1
	s_waitcnt lgkmcnt(0)
	s_waitcnt vmcnt(0)
	buffer_inv sc1
	v_mbcnt_lo_u32_b32 v2, s6, 0
	v_mbcnt_hi_u32_b32 v2, s7, v2
	v_cmp_eq_u32_e32 vcc, 0, v2
	s_and_saveexec_b64 s[8:9], vcc
	s_cbranch_execz .LBB0_85
	s_bcnt1_i32_b64 s3, s[6:7]
	v_mov_b32_e32 v3, 0x3000
	v_mov_b32_e32 v4, s3
	global_atomic_add v3, v3, v4, s[72:73] offset:1024 sc0

; __device__ __forceinline__ unsigned xb_ld(unsigned* p)              { return __hip_atomic_load(p, __ATOMIC_RELAXED, __HIP_MEMORY_SCOPE_AGENT); }
; __device__ __forceinline__ unsigned xb_add(unsigned* p, unsigned v) { return __hip_atomic_fetch_add(p, v, __ATOMIC_RELAXED, __HIP_MEMORY_SCOPE_AGENT); }
; #define XB_SPIN(cond, bar) do { unsigned _sp = 0; while (cond) { __builtin_amdgcn_s_sleep(1); \
;     if ((++_sp & 255u) == 0u) { if (xb_ld(&(bar)[XB_TMO])) break; if (_sp > XB_SPIN_CAP) { atomicAdd(&(bar)[XB_TMO], 1u); break; } } } } while (0)
; __device__ __forceinline__ void xcd_barrier(const XcdBarrier& b) {
;     ...
;             const unsigned og = xb_add(&bar[XB_TOP], 1u);
;             const unsigned tg = og / nx;
;             if (og + 1u == (tg + 1u) * nx) xb_add(&bar[XB_TOPGEN], 1u);
;             else XB_SPIN(xb_ld(&bar[XB_TOPGEN]) == tg, bar);
;             __builtin_amdgcn_fence(__ATOMIC_ACQUIRE, "agent");
;             xb_add(&bar[XB_XGEN(b.x)], 1u);
;             asm volatile("s_waitcnt vmcnt(0)" ::: "memory");
.LBB0_99:
	s_or_b64 exec, exec, s[6:7]
	v_mov_b32_e32 v1, 0x2000
	v_mov_b32_e32 v2, 1
	s_waitcnt vmcnt(0)
	global_atomic_add v1, v2, s[4:5] offset:1024
	s_waitcnt vmcnt(0)

; __device__ __forceinline__ unsigned xb_ld(unsigned* p)              { return __hip_atomic_load(p, __ATOMIC_RELAXED, __HIP_MEMORY_SCOPE_AGENT); }
; __device__ __forceinline__ unsigned xb_add(unsigned* p, unsigned v) { return __hip_atomic_fetch_add(p, v, __ATOMIC_RELAXED, __HIP_MEMORY_SCOPE_AGENT); }
; #define XB_SPIN(cond, bar) do { unsigned _sp = 0; while (cond) { __builtin_amdgcn_s_sleep(1); \
;     if ((++_sp & 255u) == 0u) { if (xb_ld(&(bar)[XB_TMO])) break; if (_sp > XB_SPIN_CAP) { atomicAdd(&(bar)[XB_TMO], 1u); break; } } } } while (0)
; __device__ __forceinline__ void xcd_barrier(const XcdBarrier& b) {
;     ...
;     if (threadIdx.x == 0) {
;         unsigned* bar = b.bar;
;         __builtin_amdgcn_s_waitcnt(0);
;         unsigned nloc = b.st[0], nx = b.st[1];
;         if (nloc == 0u) { xcd_barrier_complete(bar, b.x, nloc, nx); b.st[0] = nloc; b.st[1] = nx; }
;         const unsigned old = xb_add(&bar[XB_XSUB(b.x)], 1u);
;         const unsigned gen = old / nloc;
;         if (old + 1u == (gen + 1u) * nloc) {
;             __builtin_amdgcn_fence(__ATOMIC_RELEASE, "agent");
;             asm volatile("s_waitcnt vmcnt(0)" ::: "memory");
;             const unsigned og = xb_add(&bar[XB_TOP], 1u);
;             const unsigned tg = og / nx;
;             if (og + 1u == (tg + 1u) * nx) xb_add(&bar[XB_TOPGEN], 1u);
;             else XB_SPIN(xb_ld(&bar[XB_TOPGEN]) == tg, bar);
;             __builtin_amdgcn_fence(__ATOMIC_ACQUIRE, "agent");
;             xb_add(&bar[XB_XGEN(b.x)], 1u);
;             asm volatile("s_waitcnt vmcnt(0)" ::: "memory");
;         } else {
;             XB_SPIN(xb_ld(&bar[XB_XGEN(b.x)]) == gen, bar);
.LBB0_2846:
	s_lshl_b32 s3, s86, 8
	s_add_u32 s4, s72, s3
	s_addc_u32 s5, s73, 0
	v_mov_b32_e32 v2, 0x1000
	v_mov_b32_e32 v4, 1
	global_atomic_add v4, v2, v4, s[4:5] offset:1024 sc0
	v_cvt_f32_u32_e32 v2, v3
	v_sub_u32_e32 v5, 0, v3
	v_rcp_iflag_f32_e32 v2, v2
	s_nop 0
	v_mul_f32_e32 v2, 0x4f7ffffe, v2
	v_cvt_u32_f32_e32 v2, v2
	v_mul_lo_u32 v5, v5, v2
	v_mul_hi_u32 v5, v2, v5
	v_add_u32_e32 v2, v2, v5
	s_waitcnt vmcnt(0)
	v_mul_hi_u32 v2, v4, v2
	v_mul_lo_u32 v5, v2, v3
	v_sub_u32_e32 v5, v4, v5
	v_add_u32_e32 v6, 1, v2
	v_cmp_ge_u32_e32 vcc, v5, v3
	v_add_u32_e32 v4, 1, v4
	s_nop 0
	v_cndmask_b32_e32 v2, v2, v6, vcc
	v_sub_u32_e32 v6, v5, v3
	v_cndmask_b32_e32 v5, v5, v6, vcc
	v_add_u32_e32 v6, 1, v2
	v_cmp_ge_u32_e32 vcc, v5, v3
	s_nop 1
	v_cndmask_b32_e32 v2, v2, v6, vcc
	v_mul_lo_u32 v5, v3, v2
	v_add_u32_e32 v3, v5, v3
	v_cmp_ne_u32_e32 vcc, v4, v3
	s_and_saveexec_b64 s[6:7], vcc
	s_xor_b64 s[6:7], exec, s[6:7]
	s_cbranch_execz .LBB0_2860
	s_waitcnt lgkmcnt(0)
	buffer_inv sc1
	v_mov_b32_e32 v1, 0x2000
	global_load_dword v1, v1, s[4:5] offset:1024 sc1
	s_add_u32 s10, s4, 0x2400
	s_addc_u32 s11, s5, 0
	s_waitcnt vmcnt(0)
	v_cmp_eq_u32_e32 vcc, v1, v2
	s_and_saveexec_b64 s[8:9], vcc
	s_cbranch_execz .LBB0_2859
	s_mov_b32 s3, 1
	s_mov_b64 s[12:13], 0
	v_mov_b32_e32 v1, 0
	s_branch .LBB0_2850

; __device__ __forceinline__ unsigned xb_ld(unsigned* p)              { return __hip_atomic_load(p, __ATOMIC_RELAXED, __HIP_MEMORY_SCOPE_AGENT); }
; __device__ __forceinline__ unsigned xb_add(unsigned* p, unsigned v) { return __hip_atomic_fetch_add(p, v, __ATOMIC_RELAXED, __HIP_MEMORY_SCOPE_AGENT); }
; #define XB_SPIN(cond, bar) do { unsigned _sp = 0; while (cond) { __builtin_amdgcn_s_sleep(1); \
;     if ((++_sp & 255u) == 0u) { if (xb_ld(&(bar)[XB_TMO])) break; if (_sp > XB_SPIN_CAP) { atomicAdd(&(bar)[XB_TMO], 1u); break; } } } } while (0)
; __device__ __forceinline__ void xcd_barrier(const XcdBarrier& b) {
;     ...
;     if (threadIdx.x == 0) {
;         unsigned* bar = b.bar;
;         __builtin_amdgcn_s_waitcnt(0);
;         unsigned nloc = b.st[0], nx = b.st[1];
;         if (nloc == 0u) { xcd_barrier_complete(bar, b.x, nloc, nx); b.st[0] = nloc; b.st[1] = nx; }
;         const unsigned old = xb_add(&bar[XB_XSUB(b.x)], 1u);
;         const unsigned gen = old / nloc;
;         if (old + 1u == (gen + 1u) * nloc) {
;             __builtin_amdgcn_fence(__ATOMIC_RELEASE, "agent");
;             asm volatile("s_waitcnt vmcnt(0)" ::: "memory");
;             const unsigned og = xb_add(&bar[XB_TOP], 1u);
;             const unsigned tg = og / nx;
;             if (og + 1u == (tg + 1u) * nx) xb_add(&bar[XB_TOPGEN], 1u);
;             else XB_SPIN(xb_ld(&bar[XB_TOPGEN]) == tg, bar);
;             __builtin_amdgcn_fence(__ATOMIC_ACQUIRE, "agent");
;             xb_add(&bar[XB_XGEN(b.x)], 1u);
;             asm volatile("s_waitcnt vmcnt(0)" ::: "memory");
;         } else {
;             XB_SPIN(xb_ld(&bar[XB_XGEN(b.x)]) == gen, bar);
.LBB0_3175:
	s_lshl_b32 s2, s86, 8
	s_add_u32 s2, s72, s2
	s_addc_u32 s3, s73, 0
	v_mov_b32_e32 v2, 0x1000
	v_mov_b32_e32 v4, 1
	global_atomic_add v4, v2, v4, s[2:3] offset:1024 sc0
	v_cvt_f32_u32_e32 v2, v3
	v_sub_u32_e32 v5, 0, v3
	v_rcp_iflag_f32_e32 v2, v2
	s_nop 0
	v_mul_f32_e32 v2, 0x4f7ffffe, v2
	v_cvt_u32_f32_e32 v2, v2
	v_mul_lo_u32 v5, v5, v2
	v_mul_hi_u32 v5, v2, v5
	v_add_u32_e32 v2, v2, v5
	s_waitcnt vmcnt(0)
	v_mul_hi_u32 v2, v4, v2
	v_mul_lo_u32 v5, v2, v3
	v_sub_u32_e32 v5, v4, v5
	v_add_u32_e32 v6, 1, v2
	v_cmp_ge_u32_e32 vcc, v5, v3
	v_add_u32_e32 v4, 1, v4
	s_nop 0
	v_cndmask_b32_e32 v2, v2, v6, vcc
	v_sub_u32_e32 v6, v5, v3
	v_cndmask_b32_e32 v5, v5, v6, vcc
	v_add_u32_e32 v6, 1, v2
	v_cmp_ge_u32_e32 vcc, v5, v3
	s_nop 1
	v_cndmask_b32_e32 v2, v2, v6, vcc
	v_mul_lo_u32 v5, v3, v2
	v_add_u32_e32 v3, v5, v3
	v_cmp_ne_u32_e32 vcc, v4, v3
	s_and_saveexec_b64 s[4:5], vcc
	s_xor_b64 s[4:5], exec, s[4:5]
	s_cbranch_execz .LBB0_3189
	s_waitcnt lgkmcnt(0)
	buffer_inv sc1
	v_mov_b32_e32 v1, 0x2000
	global_load_dword v1, v1, s[2:3] offset:1024 sc1
	s_add_u32 s8, s2, 0x2400
	s_addc_u32 s9, s3, 0
	s_waitcnt vmcnt(0)
	v_cmp_eq_u32_e32 vcc, v1, v2
	s_and_saveexec_b64 s[6:7], vcc
	s_cbranch_execz .LBB0_3188
	s_mov_b32 s20, 1
	s_mov_b64 s[10:11], 0
	v_mov_b32_e32 v1, 0
	s_branch .LBB0_3179

; __device__ __forceinline__ unsigned xb_add(unsigned* p, unsigned v) { return __hip_atomic_fetch_add(p, v, __ATOMIC_RELAXED, __HIP_MEMORY_SCOPE_AGENT); }
; __device__ __forceinline__ void xcd_barrier(const XcdBarrier& b) {
;     ...
;         const unsigned gen = old / nloc;
;         if (old + 1u == (gen + 1u) * nloc) {
;             __builtin_amdgcn_fence(__ATOMIC_RELEASE, "agent");
;             asm volatile("s_waitcnt vmcnt(0)" ::: "memory");
;             const unsigned og = xb_add(&bar[XB_TOP], 1u);
.LBB0_3188:
	s_or_b64 exec, exec, s[6:7]
	s_waitcnt vmcnt(0)
	s_waitcnt vmcnt(0)
.LBB0_3189:
	s_andn2_saveexec_b64 s[4:5], s[4:5]
	s_cbranch_execz .LBB0_3207
	s_mov_b64 s[4:5], exec
	buffer_wbl2 sc1
	s_waitcnt lgkmcnt(0)
	s_waitcnt vmcnt(0)
	buffer_inv sc1
	v_mbcnt_lo_u32_b32 v2, s4, 0
	v_mbcnt_hi_u32_b32 v2, s5, v2
	v_cmp_eq_u32_e32 vcc, 0, v2
	s_and_saveexec_b64 s[6:7], vcc
	s_cbranch_execz .LBB0_3192
	s_bcnt1_i32_b64 s4, s[4:5]
	v_mov_b32_e32 v3, 0x3000
	v_mov_b32_e32 v4, s4
	global_atomic_add v3, v3, v4, s[72:73] offset:1024 sc0

; __device__ __forceinline__ unsigned xb_ld(unsigned* p)              { return __hip_atomic_load(p, __ATOMIC_RELAXED, __HIP_MEMORY_SCOPE_AGENT); }
; __device__ __forceinline__ unsigned xb_add(unsigned* p, unsigned v) { return __hip_atomic_fetch_add(p, v, __ATOMIC_RELAXED, __HIP_MEMORY_SCOPE_AGENT); }
; #define XB_SPIN(cond, bar) do { unsigned _sp = 0; while (cond) { __builtin_amdgcn_s_sleep(1); \
;     if ((++_sp & 255u) == 0u) { if (xb_ld(&(bar)[XB_TMO])) break; if (_sp > XB_SPIN_CAP) { atomicAdd(&(bar)[XB_TMO], 1u); break; } } } } while (0)
; __device__ __forceinline__ void xcd_barrier(const XcdBarrier& b) {
;     ...
;             const unsigned og = xb_add(&bar[XB_TOP], 1u);
;             const unsigned tg = og / nx;
;             if (og + 1u == (tg + 1u) * nx) xb_add(&bar[XB_TOPGEN], 1u);
;             else XB_SPIN(xb_ld(&bar[XB_TOPGEN]) == tg, bar);
;             __builtin_amdgcn_fence(__ATOMIC_ACQUIRE, "agent");
;             xb_add(&bar[XB_XGEN(b.x)], 1u);
;             asm volatile("s_waitcnt vmcnt(0)" ::: "memory");
.LBB0_3206:
	s_or_b64 exec, exec, s[4:5]
	v_mov_b32_e32 v1, 0x2000
	v_mov_b32_e32 v2, 1
	s_waitcnt vmcnt(0)
	global_atomic_add v1, v2, s[2:3] offset:1024
	s_waitcnt vmcnt(0)

; __device__ __forceinline__ unsigned xb_ld(unsigned* p)              { return __hip_atomic_load(p, __ATOMIC_RELAXED, __HIP_MEMORY_SCOPE_AGENT); }
; __device__ __forceinline__ unsigned xb_add(unsigned* p, unsigned v) { return __hip_atomic_fetch_add(p, v, __ATOMIC_RELAXED, __HIP_MEMORY_SCOPE_AGENT); }
; #define XB_SPIN(cond, bar) do { unsigned _sp = 0; while (cond) { __builtin_amdgcn_s_sleep(1); \
;     if ((++_sp & 255u) == 0u) { if (xb_ld(&(bar)[XB_TMO])) break; if (_sp > XB_SPIN_CAP) { atomicAdd(&(bar)[XB_TMO], 1u); break; } } } } while (0)
; __device__ __forceinline__ void xcd_barrier(const XcdBarrier& b) {
;     ...
;     if (threadIdx.x == 0) {
;         unsigned* bar = b.bar;
;         __builtin_amdgcn_s_waitcnt(0);
;         unsigned nloc = b.st[0], nx = b.st[1];
;         if (nloc == 0u) { xcd_barrier_complete(bar, b.x, nloc, nx); b.st[0] = nloc; b.st[1] = nx; }
;         const unsigned old = xb_add(&bar[XB_XSUB(b.x)], 1u);
;         const unsigned gen = old / nloc;
;         if (old + 1u == (gen + 1u) * nloc) {
;             __builtin_amdgcn_fence(__ATOMIC_RELEASE, "agent");
;             asm volatile("s_waitcnt vmcnt(0)" ::: "memory");
;             const unsigned og = xb_add(&bar[XB_TOP], 1u);
;             const unsigned tg = og / nx;
;             if (og + 1u == (tg + 1u) * nx) xb_add(&bar[XB_TOPGEN], 1u);
;             else XB_SPIN(xb_ld(&bar[XB_TOPGEN]) == tg, bar);
;             __builtin_amdgcn_fence(__ATOMIC_ACQUIRE, "agent");
;             xb_add(&bar[XB_XGEN(b.x)], 1u);
;             asm volatile("s_waitcnt vmcnt(0)" ::: "memory");
;         } else {
;             XB_SPIN(xb_ld(&bar[XB_XGEN(b.x)]) == gen, bar);
.LBB0_3237:
	s_lshl_b32 s2, s86, 8
	s_add_u32 s2, s72, s2
	s_addc_u32 s3, s73, 0
	v_mov_b32_e32 v1, 0x1000
	v_mov_b32_e32 v3, 1
	global_atomic_add v3, v1, v3, s[2:3] offset:1024 sc0
	v_cvt_f32_u32_e32 v1, v2
	v_sub_u32_e32 v4, 0, v2
	v_rcp_iflag_f32_e32 v1, v1
	s_nop 0
	v_mul_f32_e32 v1, 0x4f7ffffe, v1
	v_cvt_u32_f32_e32 v1, v1
	v_mul_lo_u32 v4, v4, v1
	v_mul_hi_u32 v4, v1, v4
	v_add_u32_e32 v1, v1, v4
	s_waitcnt vmcnt(0)
	v_mul_hi_u32 v1, v3, v1
	v_mul_lo_u32 v4, v1, v2
	v_sub_u32_e32 v4, v3, v4
	v_add_u32_e32 v5, 1, v1
	v_cmp_ge_u32_e32 vcc, v4, v2
	v_add_u32_e32 v3, 1, v3
	s_nop 0
	v_cndmask_b32_e32 v1, v1, v5, vcc
	v_sub_u32_e32 v5, v4, v2
	v_cndmask_b32_e32 v4, v4, v5, vcc
	v_add_u32_e32 v5, 1, v1
	v_cmp_ge_u32_e32 vcc, v4, v2
	s_nop 1
	v_cndmask_b32_e32 v1, v1, v5, vcc
	v_mul_lo_u32 v4, v2, v1
	v_add_u32_e32 v2, v4, v2
	v_cmp_ne_u32_e32 vcc, v3, v2
	s_and_saveexec_b64 s[4:5], vcc
	s_xor_b64 s[4:5], exec, s[4:5]
	s_cbranch_execz .LBB0_3251
	s_waitcnt lgkmcnt(0)
	buffer_inv sc1
	v_mov_b32_e32 v0, 0x2000
	global_load_dword v0, v0, s[2:3] offset:1024 sc1
	s_add_u32 s8, s2, 0x2400
	s_addc_u32 s9, s3, 0
	s_waitcnt vmcnt(0)
	v_cmp_eq_u32_e32 vcc, v0, v1
	s_and_saveexec_b64 s[6:7], vcc
	s_cbranch_execz .LBB0_3250
	s_mov_b32 s20, 1
	s_mov_b64 s[10:11], 0
	v_mov_b32_e32 v0, 0
	s_branch .LBB0_3241

; __device__ __forceinline__ unsigned xb_add(unsigned* p, unsigned v) { return __hip_atomic_fetch_add(p, v, __ATOMIC_RELAXED, __HIP_MEMORY_SCOPE_AGENT); }
; __device__ __forceinline__ void xcd_barrier(const XcdBarrier& b) {
;     ...
;         const unsigned gen = old / nloc;
;         if (old + 1u == (gen + 1u) * nloc) {
;             __builtin_amdgcn_fence(__ATOMIC_RELEASE, "agent");
;             asm volatile("s_waitcnt vmcnt(0)" ::: "memory");
;             const unsigned og = xb_add(&bar[XB_TOP], 1u);
.LBB0_3251:
	s_andn2_saveexec_b64 s[4:5], s[4:5]
	s_cbranch_execz .LBB0_3269
	s_mov_b64 s[4:5], exec
	buffer_wbl2 sc1
	s_waitcnt lgkmcnt(0)
	s_waitcnt vmcnt(0)
	buffer_inv sc1
	v_mbcnt_lo_u32_b32 v1, s4, 0
	v_mbcnt_hi_u32_b32 v1, s5, v1
	v_cmp_eq_u32_e32 vcc, 0, v1
	s_and_saveexec_b64 s[6:7], vcc
	s_cbranch_execz .LBB0_3254
	s_bcnt1_i32_b64 s4, s[4:5]
	v_mov_b32_e32 v2, 0x3000
	v_mov_b32_e32 v3, s4
	global_atomic_add v2, v2, v3, s[72:73] offset:1024 sc0

; __device__ __forceinline__ unsigned xb_ld(unsigned* p)              { return __hip_atomic_load(p, __ATOMIC_RELAXED, __HIP_MEMORY_SCOPE_AGENT); }
; __device__ __forceinline__ unsigned xb_add(unsigned* p, unsigned v) { return __hip_atomic_fetch_add(p, v, __ATOMIC_RELAXED, __HIP_MEMORY_SCOPE_AGENT); }
; #define XB_SPIN(cond, bar) do { unsigned _sp = 0; while (cond) { __builtin_amdgcn_s_sleep(1); \
;     if ((++_sp & 255u) == 0u) { if (xb_ld(&(bar)[XB_TMO])) break; if (_sp > XB_SPIN_CAP) { atomicAdd(&(bar)[XB_TMO], 1u); break; } } } } while (0)
; __device__ __forceinline__ void xcd_barrier(const XcdBarrier& b) {
;     ...
;             const unsigned og = xb_add(&bar[XB_TOP], 1u);
;             const unsigned tg = og / nx;
;             if (og + 1u == (tg + 1u) * nx) xb_add(&bar[XB_TOPGEN], 1u);
;             else XB_SPIN(xb_ld(&bar[XB_TOPGEN]) == tg, bar);
;             __builtin_amdgcn_fence(__ATOMIC_ACQUIRE, "agent");
;             xb_add(&bar[XB_XGEN(b.x)], 1u);
;             asm volatile("s_waitcnt vmcnt(0)" ::: "memory");
.LBB0_3268:
	s_or_b64 exec, exec, s[4:5]
	v_mov_b32_e32 v0, 0x2000
	v_mov_b32_e32 v1, 1
	s_waitcnt vmcnt(0)
	global_atomic_add v0, v1, s[2:3] offset:1024
	s_waitcnt vmcnt(0)
